# Deferred weight converter processes two adjacent 128x128 tiles per iteration (16 loads in flight, one ticket per pair)
# baseline (speedup 1.0000x reference)
; #define LAS __attribute__((address_space(3)))
; __device__ __forceinline__ void phase_prologue(const Args& a, LAS unsigned char* lds) {
;     ...
;     unsigned* cq_head = (unsigned*)(a.ws + WS_CTL) + 8192 + 768;
;     volatile LAS int* qs = (volatile LAS int*)(lds + 128 * 129 * 4);
;     int pend = 0, it = 0;
;     if (tid == 0) { qs[0] = (int)xb_add(cq_head, 1u); pend = (int)xb_add(cq_head, 1u); }
;     __syncthreads();
;     for (int u = qs[0]; u < CTOT; u = qs[it & 1]) {
;         int r = u; const float* src; int ldn, nvalid, NT, mode = 0; bf16_t* dst;
;         if (r < CJ0) { src = a.in[I_EVIN]; ldn = 6144; nvalid = 6144; NT = 48; dst = (bf16_t*)(a.ws + WS_WIN0); }
;         else if ((r -= CJ0) < CJ1) { src = a.in[I_EVOUT]; ldn = 2048; nvalid = 2048; NT = 16; dst = (bf16_t*)(a.ws + WS_WOUT0); }
;         else if ((r -= CJ1) < CJ2) { src = a.in[I_ODIN]; ldn = 6176; nvalid = 6176; NT = 50; dst = (bf16_t*)(a.ws + WS_WIN1); }
;         else if ((r -= CJ2) < CJ3) { src = a.in[I_ODOUT]; ldn = 2048; nvalid = 2048; NT = 16; dst = (bf16_t*)(a.ws + WS_WOUT1); }
;         else { r -= CJ3; const int which = r / CJM; r -= which * CJM; const int mtx = r >> 8; r &= 255; ldn = 2048; nvalid = 2048; NT = 16;
;             if (which == 0) { src = a.in[I_WGATE] + (size_t)mtx * 2048 * 2048; dst = (bf16_t*)(a.ws + WS_WGU) + (size_t)mtx * 4096 * 2048; mode = 1; }
;             else if (which == 1) { src = a.in[I_WUP] + (size_t)mtx * 2048 * 2048; dst = (bf16_t*)(a.ws + WS_WGU) + (size_t)mtx * 4096 * 2048; mode = 2; }
;             else { src = a.in[I_WDOWN] + (size_t)mtx * 2048 * 2048; dst = (bf16_t*)(a.ws + WS_WDN) + (size_t)mtx * 2048 * 2048; } }
;         const int kt = r / NT, ntl = r % NT, k0 = kt * 128, n0 = ntl * 128;
;         const int drow0 = mode == 0 ? n0 : (ntl * 256 + (mode == 2 ? 128 : 0));
;         f32x4 v[8];
; #pragma unroll
;         for (int i = 0; i < 8; ++i) { const int id = tid + 512 * i, row = id >> 5, c4 = id & 31, n = n0 + c4 * 4;
;             v[i] = (f32x4){0.f, 0.f, 0.f, 0.f};
;             if (n < nvalid) v[i] = *(const f32x4*)(src + (size_t)(k0 + row) * ldn + n); }
; #pragma unroll
;         for (int i = 0; i < 8; ++i) { const int id = tid + 512 * i, row = id >> 5, c4 = id & 31;
;             LAS float* tp = tile + row * 129 + c4 * 4; tp[0] = v[i][0]; tp[1] = v[i][1]; tp[2] = v[i][2]; tp[3] = v[i][3]; }
;         lds_barrier();
; #pragma unroll
.Lcva_entry:
	s_waitcnt vmcnt(0) lgkmcnt(0)
	s_barrier
	v_mov_b32_e32 v119, 1
	v_mov_b32_e32 v208, 2
	v_mov_b32_e32 v120, 0x9000
	v_mov_b32_e32 v121, 0x9100
	v_mov_b32_e32 v122, 0
	v_mov_b32_e32 v125, 0x10200
	s_mov_b32 s25, 0
	v_cmp_eq_u32_e32 vcc, 0, v0
	s_and_saveexec_b64 s[34:35], vcc
	s_cbranch_execz .Lcva_f0
	global_atomic_add v124, v121, v122, s[94:95] sc0
	s_waitcnt vmcnt(0)
	ds_write_b32 v125, v124 offset:4
.Lcva_f0:
	s_mov_b64 exec, s[34:35]
	s_waitcnt lgkmcnt(0)
	s_barrier
	ds_read_b32 v127, v125 offset:4
	s_waitcnt lgkmcnt(0)
	v_readfirstlane_b32 s25, v127
	s_cmpk_ge_u32 s25, 0x1
	s_cbranch_scc1 .Lcva_done
	s_barrier
	v_lshrrev_b32_e32 v104, 5, v0
	v_and_b32_e32 v126, 31, v0
	v_lshlrev_b32_e32 v105, 13, v104
	v_lshl_add_u32 v105, v126, 4, v105
	v_add_u32_e32 v106, 0x20000, v105
	v_add_u32_e32 v107, 0x40000, v105
	v_add_u32_e32 v108, 0x60000, v105
	v_add_u32_e32 v109, 0x80000, v105
	v_add_u32_e32 v110, 0xa0000, v105
	v_add_u32_e32 v111, 0xc0000, v105
	v_add_u32_e32 v112, 0xe0000, v105
	v_mul_u32_u24_e32 v113, 0x204, v104
	v_lshl_add_u32 v113, v126, 4, v113
	v_lshrrev_b32_e32 v127, 4, v0
	v_and_b32_e32 v126, 15, v0
	v_mul_u32_u24_e32 v114, 0x1020, v126
	v_lshl_add_u32 v114, v127, 2, v114
	v_lshlrev_b32_e32 v115, 12, v127
	v_lshl_add_u32 v115, v126, 4, v115
	v_add_u32_e32 v116, 0x20000, v115
	v_add_u32_e32 v117, 0x40000, v115
	v_add_u32_e32 v118, 0x60000, v115
	v_add_u32_e32 v209, 0x10240, v113
	v_add_u32_e32 v210, 0x10240, v114
	v_readlane_b32 s42, v254, 27
	v_readlane_b32 s43, v254, 28
	s_sub_u32 s42, s42, 0x28
	s_subb_u32 s43, s43, 0
	s_load_dwordx2 s[40:41], s[42:43], 0x0
	s_waitcnt lgkmcnt(0)
	v_cmp_eq_u32_e32 vcc, 0, v0
	s_and_saveexec_b64 s[34:35], vcc
	s_cbranch_execz .Lcva_t0a
	global_atomic_add v123, v120, v208, s[94:95] sc0
	s_waitcnt vmcnt(0)
	ds_write_b32 v125, v123
	ds_write_b32 v125, v122 offset:4

; __device__ __forceinline__ void lds_barrier() { asm volatile("s_waitcnt lgkmcnt(0)" ::: "memory"); __builtin_amdgcn_s_barrier(); asm volatile("" ::: "memory"); }
; __device__ __forceinline__ unsigned xb_add(unsigned* p, unsigned v) { return __hip_atomic_fetch_add(p, v, __ATOMIC_RELAXED, __HIP_MEMORY_SCOPE_AGENT); }
; __device__ __forceinline__ void phase_prologue(const Args& a, LAS unsigned char* lds) {
;     ...
;         ++it;
;         if (tid == 0) { qs[it & 1] = pend; pend = (int)xb_add(cq_head, 1u); }
;         lds_barrier();
.Lcva_loop:
	ds_read_b32 v126, v125
	ds_read_b32 v127, v125 offset:4
	s_waitcnt lgkmcnt(0)
	v_readfirstlane_b32 s24, v126
	v_readfirstlane_b32 s25, v127
	s_cmpk_gt_u32 s24, 0x1fff
	s_cbranch_scc1 .Lcva_done
	s_cmpk_ge_u32 s25, 0x1
	s_cbranch_scc1 .Lcva_nopf
	v_cmp_eq_u32_e32 vcc, 0, v0
	s_and_saveexec_b64 s[34:35], vcc
	s_cbranch_execz .Lcva_t0b
	global_atomic_add v123, v120, v208, s[94:95] sc0
	global_atomic_add v124, v121, v122, s[94:95] sc0

; #define LAS __attribute__((address_space(3)))
; __device__ __forceinline__ void lds_barrier() { asm volatile("s_waitcnt lgkmcnt(0)" ::: "memory"); __builtin_amdgcn_s_barrier(); asm volatile("" ::: "memory"); }
; __device__ __forceinline__ void phase_prologue(const Args& a, LAS unsigned char* lds) {
;     ...
;         const int kt = r / NT, ntl = r % NT, k0 = kt * 128, n0 = ntl * 128;
;         const int drow0 = mode == 0 ? n0 : (ntl * 256 + (mode == 2 ? 128 : 0));
;         f32x4 v[8];
; #pragma unroll
;         for (int i = 0; i < 8; ++i) { const int id = tid + 512 * i, row = id >> 5, c4 = id & 31, n = n0 + c4 * 4;
;             v[i] = (f32x4){0.f, 0.f, 0.f, 0.f};
;             if (n < nvalid) v[i] = *(const f32x4*)(src + (size_t)(k0 + row) * ldn + n); }
; #pragma unroll
;         for (int i = 0; i < 8; ++i) { const int id = tid + 512 * i, row = id >> 5, c4 = id & 31;
;             LAS float* tp = tile + row * 129 + c4 * 4; tp[0] = v[i][0]; tp[1] = v[i][1]; tp[2] = v[i][2]; tp[3] = v[i][3]; }
;         lds_barrier();
.Lcva_nopf:
	s_lshr_b32 s36, s24, 12
	s_bfe_u32 s30, s24, 0x40008
	s_add_i32 s30, s30, 16
	s_lshl_b32 s30, s30, 24
	s_bfe_u32 s31, s24, 0x40004
	s_and_b32 s32, s24, 15
	v_readlane_b32 s26, v254, 43
	v_readlane_b32 s27, v254, 44
	s_cmp_lg_u32 s36, 0
	s_cselect_b32 s26, s40, s26
	s_cselect_b32 s27, s41, s27
	s_lshl_b32 s33, s31, 20
	s_add_i32 s33, s33, s30
	s_lshl_b32 s37, s32, 9
	s_add_i32 s33, s33, s37
	s_add_u32 s26, s26, s33
	s_addc_u32 s27, s27, 0
	v_readlane_b32 s28, v254, 25
	v_readlane_b32 s29, v254, 26
	s_lshl_b32 s33, s32, 20
	s_add_i32 s33, s33, s30
	s_lshl_b32 s37, s36, 19
	s_add_i32 s33, s33, s37
	s_lshl_b32 s37, s31, 8
	s_add_i32 s33, s33, s37
	s_add_u32 s28, s28, s33
	s_addc_u32 s29, s29, 0
	s_add_u32 s44, s28, 0x100000
	s_addc_u32 s45, s29, 0
	global_load_dwordx4 v[128:131], v105, s[26:27]
	global_load_dwordx4 v[132:135], v106, s[26:27]
	global_load_dwordx4 v[136:139], v107, s[26:27]
	global_load_dwordx4 v[140:143], v108, s[26:27]
	global_load_dwordx4 v[144:147], v109, s[26:27]
	global_load_dwordx4 v[148:151], v110, s[26:27]
	global_load_dwordx4 v[152:155], v111, s[26:27]
	global_load_dwordx4 v[156:159], v112, s[26:27]
	global_load_dwordx4 v[176:179], v105, s[26:27] offset:512
	global_load_dwordx4 v[180:183], v106, s[26:27] offset:512
	global_load_dwordx4 v[184:187], v107, s[26:27] offset:512
	global_load_dwordx4 v[188:191], v108, s[26:27] offset:512
	global_load_dwordx4 v[192:195], v109, s[26:27] offset:512
	global_load_dwordx4 v[196:199], v110, s[26:27] offset:512
	global_load_dwordx4 v[200:203], v111, s[26:27] offset:512
	global_load_dwordx4 v[204:207], v112, s[26:27] offset:512
	s_waitcnt vmcnt(15)
	ds_write_b32 v113, v128
	ds_write_b32 v113, v129 offset:4
	ds_write_b32 v113, v130 offset:8
	ds_write_b32 v113, v131 offset:12
	s_waitcnt vmcnt(14)
	ds_write_b32 v113, v132 offset:8256
	ds_write_b32 v113, v133 offset:8260
	ds_write_b32 v113, v134 offset:8264
	ds_write_b32 v113, v135 offset:8268
	s_waitcnt vmcnt(13)
	ds_write_b32 v113, v136 offset:16512
	ds_write_b32 v113, v137 offset:16516
	ds_write_b32 v113, v138 offset:16520
	ds_write_b32 v113, v139 offset:16524
	s_waitcnt vmcnt(12)
	ds_write_b32 v113, v140 offset:24768
	ds_write_b32 v113, v141 offset:24772
	ds_write_b32 v113, v142 offset:24776
	ds_write_b32 v113, v143 offset:24780
	s_waitcnt vmcnt(11)
	ds_write_b32 v113, v144 offset:33024
	ds_write_b32 v113, v145 offset:33028
	ds_write_b32 v113, v146 offset:33032
	ds_write_b32 v113, v147 offset:33036
	s_waitcnt vmcnt(10)
	ds_write_b32 v113, v148 offset:41280
	ds_write_b32 v113, v149 offset:41284
	ds_write_b32 v113, v150 offset:41288
	ds_write_b32 v113, v151 offset:41292
	s_waitcnt vmcnt(9)
	ds_write_b32 v113, v152 offset:49536
	ds_write_b32 v113, v153 offset:49540
	ds_write_b32 v113, v154 offset:49544
	ds_write_b32 v113, v155 offset:49548
	s_waitcnt vmcnt(8)
	ds_write_b32 v113, v156 offset:57792
	ds_write_b32 v113, v157 offset:57796
	ds_write_b32 v113, v158 offset:57800
	ds_write_b32 v113, v159 offset:57804
	s_waitcnt vmcnt(7)
	ds_write_b32 v209, v176
	ds_write_b32 v209, v177 offset:4
	ds_write_b32 v209, v178 offset:8
	ds_write_b32 v209, v179 offset:12
	s_waitcnt vmcnt(6)
	ds_write_b32 v209, v180 offset:8256
	ds_write_b32 v209, v181 offset:8260
	ds_write_b32 v209, v182 offset:8264
	ds_write_b32 v209, v183 offset:8268
	s_waitcnt vmcnt(5)
	ds_write_b32 v209, v184 offset:16512
	ds_write_b32 v209, v185 offset:16516
	ds_write_b32 v209, v186 offset:16520
	ds_write_b32 v209, v187 offset:16524
	s_waitcnt vmcnt(4)
	ds_write_b32 v209, v188 offset:24768
	ds_write_b32 v209, v189 offset:24772
	ds_write_b32 v209, v190 offset:24776
	ds_write_b32 v209, v191 offset:24780
	s_waitcnt vmcnt(3)
	ds_write_b32 v209, v192 offset:33024
	ds_write_b32 v209, v193 offset:33028
	ds_write_b32 v209, v194 offset:33032
	ds_write_b32 v209, v195 offset:33036
	s_waitcnt vmcnt(2)
	ds_write_b32 v209, v196 offset:41280
	ds_write_b32 v209, v197 offset:41284
	ds_write_b32 v209, v198 offset:41288
	ds_write_b32 v209, v199 offset:41292
	s_waitcnt vmcnt(1)
	ds_write_b32 v209, v200 offset:49536
	ds_write_b32 v209, v201 offset:49540
	ds_write_b32 v209, v202 offset:49544
	ds_write_b32 v209, v203 offset:49548
	s_waitcnt vmcnt(0)
	ds_write_b32 v209, v204 offset:57792
	ds_write_b32 v209, v205 offset:57796
	ds_write_b32 v209, v206 offset:57800
	ds_write_b32 v209, v207 offset:57804
	s_waitcnt lgkmcnt(0)
	s_barrier
; #define LAS __attribute__((address_space(3)))
; __device__ __forceinline__ void lds_barrier() { asm volatile("s_waitcnt lgkmcnt(0)" ::: "memory"); __builtin_amdgcn_s_barrier(); asm volatile("" ::: "memory"); }
; __device__ __forceinline__ void phase_prologue(const Args& a, LAS unsigned char* lds) {
;     ...
;         lds_barrier();
; #pragma unroll
;         for (int i = 0; i < 4; ++i) { const int piece = tid + 512 * i, nl = piece >> 4, kg = piece & 15; const LAS float* s = tile + (kg * 8) * 129 + nl;
;             u32x4 o; o.x = pk2(s[0], s[129]); o.y = pk2(s[258], s[387]); o.z = pk2(s[516], s[645]); o.w = pk2(s[774], s[903]);
;             *(u32x4*)(dst + (size_t)(drow0 + nl) * 2048 + k0 + kg * 8) = o; }
	ds_read_b32 v160, v114
	ds_read_b32 v161, v114 offset:516
	ds_read_b32 v162, v114 offset:1032
	ds_read_b32 v163, v114 offset:1548
	ds_read_b32 v164, v114 offset:2064
	ds_read_b32 v165, v114 offset:2580
	ds_read_b32 v166, v114 offset:3096
	ds_read_b32 v167, v114 offset:3612
	s_waitcnt lgkmcnt(0)
	v_cvt_pk_bf16_f32 v168, v160, v161
	v_cvt_pk_bf16_f32 v169, v162, v163
	v_cvt_pk_bf16_f32 v170, v164, v165
	v_cvt_pk_bf16_f32 v171, v166, v167
	global_store_dwordx4 v115, v[168:171], s[28:29]
	ds_read_b32 v160, v114 offset:128
	ds_read_b32 v161, v114 offset:644
	ds_read_b32 v162, v114 offset:1160
	ds_read_b32 v163, v114 offset:1676
	ds_read_b32 v164, v114 offset:2192
	ds_read_b32 v165, v114 offset:2708
	ds_read_b32 v166, v114 offset:3224
	ds_read_b32 v167, v114 offset:3740
	s_waitcnt lgkmcnt(0)
	v_cvt_pk_bf16_f32 v172, v160, v161
	v_cvt_pk_bf16_f32 v173, v162, v163
	v_cvt_pk_bf16_f32 v174, v164, v165
	v_cvt_pk_bf16_f32 v175, v166, v167
	global_store_dwordx4 v116, v[172:175], s[28:29]
	ds_read_b32 v160, v114 offset:256
	ds_read_b32 v161, v114 offset:772
	ds_read_b32 v162, v114 offset:1288
	ds_read_b32 v163, v114 offset:1804
	ds_read_b32 v164, v114 offset:2320
	ds_read_b32 v165, v114 offset:2836
	ds_read_b32 v166, v114 offset:3352
	ds_read_b32 v167, v114 offset:3868
	s_waitcnt lgkmcnt(0)
	v_cvt_pk_bf16_f32 v168, v160, v161
	v_cvt_pk_bf16_f32 v169, v162, v163
	v_cvt_pk_bf16_f32 v170, v164, v165
	v_cvt_pk_bf16_f32 v171, v166, v167
	global_store_dwordx4 v117, v[168:171], s[28:29]
	ds_read_b32 v160, v114 offset:384
	ds_read_b32 v161, v114 offset:900
	ds_read_b32 v162, v114 offset:1416
	ds_read_b32 v163, v114 offset:1932
	ds_read_b32 v164, v114 offset:2448
	ds_read_b32 v165, v114 offset:2964
	ds_read_b32 v166, v114 offset:3480
	ds_read_b32 v167, v114 offset:3996
	s_waitcnt lgkmcnt(0)
	v_cvt_pk_bf16_f32 v172, v160, v161
	v_cvt_pk_bf16_f32 v173, v162, v163
	v_cvt_pk_bf16_f32 v174, v164, v165
	v_cvt_pk_bf16_f32 v175, v166, v167
	global_store_dwordx4 v118, v[172:175], s[28:29]
	ds_read_b32 v160, v210
	ds_read_b32 v161, v210 offset:516
	ds_read_b32 v162, v210 offset:1032
	ds_read_b32 v163, v210 offset:1548
	ds_read_b32 v164, v210 offset:2064
	ds_read_b32 v165, v210 offset:2580
	ds_read_b32 v166, v210 offset:3096
	ds_read_b32 v167, v210 offset:3612
	s_waitcnt lgkmcnt(0)
	v_cvt_pk_bf16_f32 v168, v160, v161
	v_cvt_pk_bf16_f32 v169, v162, v163
	v_cvt_pk_bf16_f32 v170, v164, v165
	v_cvt_pk_bf16_f32 v171, v166, v167
	global_store_dwordx4 v115, v[168:171], s[44:45]
	ds_read_b32 v160, v210 offset:128
	ds_read_b32 v161, v210 offset:644
	ds_read_b32 v162, v210 offset:1160
	ds_read_b32 v163, v210 offset:1676
	ds_read_b32 v164, v210 offset:2192
	ds_read_b32 v165, v210 offset:2708
	ds_read_b32 v166, v210 offset:3224
	ds_read_b32 v167, v210 offset:3740
	s_waitcnt lgkmcnt(0)
	v_cvt_pk_bf16_f32 v172, v160, v161
	v_cvt_pk_bf16_f32 v173, v162, v163
	v_cvt_pk_bf16_f32 v174, v164, v165
	v_cvt_pk_bf16_f32 v175, v166, v167
	global_store_dwordx4 v116, v[172:175], s[44:45]
	ds_read_b32 v160, v210 offset:256
	ds_read_b32 v161, v210 offset:772
	ds_read_b32 v162, v210 offset:1288
	ds_read_b32 v163, v210 offset:1804
	ds_read_b32 v164, v210 offset:2320
	ds_read_b32 v165, v210 offset:2836
	ds_read_b32 v166, v210 offset:3352
	ds_read_b32 v167, v210 offset:3868
	s_waitcnt lgkmcnt(0)
	v_cvt_pk_bf16_f32 v168, v160, v161
	v_cvt_pk_bf16_f32 v169, v162, v163
	v_cvt_pk_bf16_f32 v170, v164, v165
	v_cvt_pk_bf16_f32 v171, v166, v167
	global_store_dwordx4 v117, v[168:171], s[44:45]
	ds_read_b32 v160, v210 offset:384
	ds_read_b32 v161, v210 offset:900
	ds_read_b32 v162, v210 offset:1416
	ds_read_b32 v163, v210 offset:1932
	ds_read_b32 v164, v210 offset:2448
	ds_read_b32 v165, v210 offset:2964
	ds_read_b32 v166, v210 offset:3480
	ds_read_b32 v167, v210 offset:3996
	s_waitcnt lgkmcnt(0)
	v_cvt_pk_bf16_f32 v172, v160, v161
	v_cvt_pk_bf16_f32 v173, v162, v163
	v_cvt_pk_bf16_f32 v174, v164, v165
	v_cvt_pk_bf16_f32 v175, v166, v167
	global_store_dwordx4 v118, v[172:175], s[44:45]
	s_cmpk_ge_u32 s25, 0x1
	s_cbranch_scc1 .Lcva_done
	v_cmp_eq_u32_e32 vcc, 0, v0
	s_and_saveexec_b64 s[34:35], vcc
	s_cbranch_execz .Lcva_t0c
	s_waitcnt vmcnt(0)
	ds_write_b32 v125, v123
	ds_write_b32 v125, v124 offset:4

; #define LAS __attribute__((address_space(3)))
; __device__ __forceinline__ void phase_prologue(const Args& a, LAS unsigned char* lds) {
;     ...
;     unsigned* cq_head = (unsigned*)(a.ws + WS_CTL) + 8192 + 768;
;     volatile LAS int* qs = (volatile LAS int*)(lds + 128 * 129 * 4);
;     int pend = 0, it = 0;
;     if (tid == 0) { qs[0] = (int)xb_add(cq_head, 1u); pend = (int)xb_add(cq_head, 1u); }
;     __syncthreads();
;     for (int u = qs[0]; u < CTOT; u = qs[it & 1]) {
;         int r = u; const float* src; int ldn, nvalid, NT, mode = 0; bf16_t* dst;
;         if (r < CJ0) { src = a.in[I_EVIN]; ldn = 6144; nvalid = 6144; NT = 48; dst = (bf16_t*)(a.ws + WS_WIN0); }
;         else if ((r -= CJ0) < CJ1) { src = a.in[I_EVOUT]; ldn = 2048; nvalid = 2048; NT = 16; dst = (bf16_t*)(a.ws + WS_WOUT0); }
;         else if ((r -= CJ1) < CJ2) { src = a.in[I_ODIN]; ldn = 6176; nvalid = 6176; NT = 50; dst = (bf16_t*)(a.ws + WS_WIN1); }
;         else if ((r -= CJ2) < CJ3) { src = a.in[I_ODOUT]; ldn = 2048; nvalid = 2048; NT = 16; dst = (bf16_t*)(a.ws + WS_WOUT1); }
;         else { r -= CJ3; const int which = r / CJM; r -= which * CJM; const int mtx = r >> 8; r &= 255; ldn = 2048; nvalid = 2048; NT = 16;
;             if (which == 0) { src = a.in[I_WGATE] + (size_t)mtx * 2048 * 2048; dst = (bf16_t*)(a.ws + WS_WGU) + (size_t)mtx * 4096 * 2048; mode = 1; }
;             else if (which == 1) { src = a.in[I_WUP] + (size_t)mtx * 2048 * 2048; dst = (bf16_t*)(a.ws + WS_WGU) + (size_t)mtx * 4096 * 2048; mode = 2; }
;             else { src = a.in[I_WDOWN] + (size_t)mtx * 2048 * 2048; dst = (bf16_t*)(a.ws + WS_WDN) + (size_t)mtx * 2048 * 2048; } }
;         const int kt = r / NT, ntl = r % NT, k0 = kt * 128, n0 = ntl * 128;
;         const int drow0 = mode == 0 ? n0 : (ntl * 256 + (mode == 2 ? 128 : 0));
;         f32x4 v[8];
; #pragma unroll
;         for (int i = 0; i < 8; ++i) { const int id = tid + 512 * i, row = id >> 5, c4 = id & 31, n = n0 + c4 * 4;
;             v[i] = (f32x4){0.f, 0.f, 0.f, 0.f};
;             if (n < nvalid) v[i] = *(const f32x4*)(src + (size_t)(k0 + row) * ldn + n); }
; #pragma unroll
;         for (int i = 0; i < 8; ++i) { const int id = tid + 512 * i, row = id >> 5, c4 = id & 31;
;             LAS float* tp = tile + row * 129 + c4 * 4; tp[0] = v[i][0]; tp[1] = v[i][1]; tp[2] = v[i][2]; tp[3] = v[i][3]; }
;         lds_barrier();
; #pragma unroll
.LBB0_1442:
.Lcvb_entry:
	s_waitcnt vmcnt(0) lgkmcnt(0)
	s_barrier
	v_mov_b32_e32 v119, 1
	v_mov_b32_e32 v208, 2
	v_mov_b32_e32 v120, 0x9000
	v_mov_b32_e32 v121, 0x9300
	v_mov_b32_e32 v122, 0
	v_mov_b32_e32 v125, 0x10200
	s_mov_b32 s25, 0
	v_cmp_eq_u32_e32 vcc, 0, v0
	s_and_saveexec_b64 s[34:35], vcc
	s_cbranch_execz .Lcvb_f0
	global_atomic_add v124, v121, v119, s[94:95] sc0
	s_waitcnt vmcnt(0)
	v_add_u32_e32 v124, 1, v124
	ds_write_b32 v125, v124 offset:4
.Lcvb_f0:
	s_mov_b64 exec, s[34:35]
	s_waitcnt lgkmcnt(0)
	s_barrier
	ds_read_b32 v127, v125 offset:4
	s_waitcnt lgkmcnt(0)
	v_readfirstlane_b32 s25, v127
	s_cmpk_ge_u32 s25, 0x100
	s_cbranch_scc1 .Lcvb_done
	s_barrier
	v_lshrrev_b32_e32 v104, 5, v0
	v_and_b32_e32 v126, 31, v0
	v_lshlrev_b32_e32 v105, 13, v104
	v_lshl_add_u32 v105, v126, 4, v105
	v_add_u32_e32 v106, 0x20000, v105
	v_add_u32_e32 v107, 0x40000, v105
	v_add_u32_e32 v108, 0x60000, v105
	v_add_u32_e32 v109, 0x80000, v105
	v_add_u32_e32 v110, 0xa0000, v105
	v_add_u32_e32 v111, 0xc0000, v105
	v_add_u32_e32 v112, 0xe0000, v105
	v_mul_u32_u24_e32 v113, 0x204, v104
	v_lshl_add_u32 v113, v126, 4, v113
	v_lshrrev_b32_e32 v127, 4, v0
	v_and_b32_e32 v126, 15, v0
	v_mul_u32_u24_e32 v114, 0x1020, v126
	v_lshl_add_u32 v114, v127, 2, v114
	v_lshlrev_b32_e32 v115, 12, v127
	v_lshl_add_u32 v115, v126, 4, v115
	v_add_u32_e32 v116, 0x20000, v115
	v_add_u32_e32 v117, 0x40000, v115
	v_add_u32_e32 v118, 0x60000, v115
	v_add_u32_e32 v209, 0x10240, v113
	v_add_u32_e32 v210, 0x10240, v114
	v_readlane_b32 s42, v254, 27
	v_readlane_b32 s43, v254, 28
	s_sub_u32 s42, s42, 0x28
	s_subb_u32 s43, s43, 0
	s_load_dwordx2 s[40:41], s[42:43], 0x0
	s_waitcnt lgkmcnt(0)
	v_cmp_eq_u32_e32 vcc, 0, v0
	s_and_saveexec_b64 s[34:35], vcc
	s_cbranch_execz .Lcvb_t0a
	global_atomic_add v123, v120, v208, s[94:95] sc0
	s_waitcnt vmcnt(0)
	ds_write_b32 v125, v123
	ds_write_b32 v125, v122 offset:4

; __device__ __forceinline__ void lds_barrier() { asm volatile("s_waitcnt lgkmcnt(0)" ::: "memory"); __builtin_amdgcn_s_barrier(); asm volatile("" ::: "memory"); }
; __device__ __forceinline__ unsigned xb_add(unsigned* p, unsigned v) { return __hip_atomic_fetch_add(p, v, __ATOMIC_RELAXED, __HIP_MEMORY_SCOPE_AGENT); }
; __device__ __forceinline__ void phase_prologue(const Args& a, LAS unsigned char* lds) {
;     ...
;         ++it;
;         if (tid == 0) { qs[it & 1] = pend; pend = (int)xb_add(cq_head, 1u); }
;         lds_barrier();
.Lcvb_loop:
	ds_read_b32 v126, v125
	ds_read_b32 v127, v125 offset:4
	s_waitcnt lgkmcnt(0)
	v_readfirstlane_b32 s24, v126
	v_readfirstlane_b32 s25, v127
	s_cmpk_gt_u32 s24, 0x1fff
	s_cbranch_scc1 .Lcvb_done
	s_cmpk_ge_u32 s25, 0x100
	s_cbranch_scc1 .Lcvb_nopf
	v_cmp_eq_u32_e32 vcc, 0, v0
	s_and_saveexec_b64 s[34:35], vcc
	s_cbranch_execz .Lcvb_t0b
	global_atomic_add v123, v120, v208, s[94:95] sc0
	global_atomic_add v124, v121, v122, s[94:95] sc0

; #define LAS __attribute__((address_space(3)))
; __device__ __forceinline__ void lds_barrier() { asm volatile("s_waitcnt lgkmcnt(0)" ::: "memory"); __builtin_amdgcn_s_barrier(); asm volatile("" ::: "memory"); }
; __device__ __forceinline__ void phase_prologue(const Args& a, LAS unsigned char* lds) {
;     ...
;         const int kt = r / NT, ntl = r % NT, k0 = kt * 128, n0 = ntl * 128;
;         const int drow0 = mode == 0 ? n0 : (ntl * 256 + (mode == 2 ? 128 : 0));
;         f32x4 v[8];
; #pragma unroll
;         for (int i = 0; i < 8; ++i) { const int id = tid + 512 * i, row = id >> 5, c4 = id & 31, n = n0 + c4 * 4;
;             v[i] = (f32x4){0.f, 0.f, 0.f, 0.f};
;             if (n < nvalid) v[i] = *(const f32x4*)(src + (size_t)(k0 + row) * ldn + n); }
; #pragma unroll
;         for (int i = 0; i < 8; ++i) { const int id = tid + 512 * i, row = id >> 5, c4 = id & 31;
;             LAS float* tp = tile + row * 129 + c4 * 4; tp[0] = v[i][0]; tp[1] = v[i][1]; tp[2] = v[i][2]; tp[3] = v[i][3]; }
;         lds_barrier();
.Lcvb_nopf:
	s_lshr_b32 s36, s24, 12
	s_bfe_u32 s30, s24, 0x40008
	s_add_i32 s30, s30, 16
	s_lshl_b32 s30, s30, 24
	s_bfe_u32 s31, s24, 0x40004
	s_and_b32 s32, s24, 15
	v_readlane_b32 s26, v254, 43
	v_readlane_b32 s27, v254, 44
	s_cmp_lg_u32 s36, 0
	s_cselect_b32 s26, s40, s26
	s_cselect_b32 s27, s41, s27
	s_lshl_b32 s33, s31, 20
	s_add_i32 s33, s33, s30
	s_lshl_b32 s37, s32, 9
	s_add_i32 s33, s33, s37
	s_add_u32 s26, s26, s33
	s_addc_u32 s27, s27, 0
	v_readlane_b32 s28, v254, 25
	v_readlane_b32 s29, v254, 26
	s_lshl_b32 s33, s32, 20
	s_add_i32 s33, s33, s30
	s_lshl_b32 s37, s36, 19
	s_add_i32 s33, s33, s37
	s_lshl_b32 s37, s31, 8
	s_add_i32 s33, s33, s37
	s_add_u32 s28, s28, s33
	s_addc_u32 s29, s29, 0
	s_add_u32 s44, s28, 0x100000
	s_addc_u32 s45, s29, 0
	global_load_dwordx4 v[128:131], v105, s[26:27]
	global_load_dwordx4 v[132:135], v106, s[26:27]
	global_load_dwordx4 v[136:139], v107, s[26:27]
	global_load_dwordx4 v[140:143], v108, s[26:27]
	global_load_dwordx4 v[144:147], v109, s[26:27]
	global_load_dwordx4 v[148:151], v110, s[26:27]
	global_load_dwordx4 v[152:155], v111, s[26:27]
	global_load_dwordx4 v[156:159], v112, s[26:27]
	global_load_dwordx4 v[176:179], v105, s[26:27] offset:512
	global_load_dwordx4 v[180:183], v106, s[26:27] offset:512
	global_load_dwordx4 v[184:187], v107, s[26:27] offset:512
	global_load_dwordx4 v[188:191], v108, s[26:27] offset:512
	global_load_dwordx4 v[192:195], v109, s[26:27] offset:512
	global_load_dwordx4 v[196:199], v110, s[26:27] offset:512
	global_load_dwordx4 v[200:203], v111, s[26:27] offset:512
	global_load_dwordx4 v[204:207], v112, s[26:27] offset:512
	s_waitcnt vmcnt(15)
	ds_write_b32 v113, v128
	ds_write_b32 v113, v129 offset:4
	ds_write_b32 v113, v130 offset:8
	ds_write_b32 v113, v131 offset:12
	s_waitcnt vmcnt(14)
	ds_write_b32 v113, v132 offset:8256
	ds_write_b32 v113, v133 offset:8260
	ds_write_b32 v113, v134 offset:8264
	ds_write_b32 v113, v135 offset:8268
	s_waitcnt vmcnt(13)
	ds_write_b32 v113, v136 offset:16512
	ds_write_b32 v113, v137 offset:16516
	ds_write_b32 v113, v138 offset:16520
	ds_write_b32 v113, v139 offset:16524
	s_waitcnt vmcnt(12)
	ds_write_b32 v113, v140 offset:24768
	ds_write_b32 v113, v141 offset:24772
	ds_write_b32 v113, v142 offset:24776
	ds_write_b32 v113, v143 offset:24780
	s_waitcnt vmcnt(11)
	ds_write_b32 v113, v144 offset:33024
	ds_write_b32 v113, v145 offset:33028
	ds_write_b32 v113, v146 offset:33032
	ds_write_b32 v113, v147 offset:33036
	s_waitcnt vmcnt(10)
	ds_write_b32 v113, v148 offset:41280
	ds_write_b32 v113, v149 offset:41284
	ds_write_b32 v113, v150 offset:41288
	ds_write_b32 v113, v151 offset:41292
	s_waitcnt vmcnt(9)
	ds_write_b32 v113, v152 offset:49536
	ds_write_b32 v113, v153 offset:49540
	ds_write_b32 v113, v154 offset:49544
	ds_write_b32 v113, v155 offset:49548
	s_waitcnt vmcnt(8)
	ds_write_b32 v113, v156 offset:57792
	ds_write_b32 v113, v157 offset:57796
	ds_write_b32 v113, v158 offset:57800
	ds_write_b32 v113, v159 offset:57804
	s_waitcnt vmcnt(7)
	ds_write_b32 v209, v176
	ds_write_b32 v209, v177 offset:4
	ds_write_b32 v209, v178 offset:8
	ds_write_b32 v209, v179 offset:12
	s_waitcnt vmcnt(6)
	ds_write_b32 v209, v180 offset:8256
	ds_write_b32 v209, v181 offset:8260
	ds_write_b32 v209, v182 offset:8264
	ds_write_b32 v209, v183 offset:8268
	s_waitcnt vmcnt(5)
	ds_write_b32 v209, v184 offset:16512
	ds_write_b32 v209, v185 offset:16516
	ds_write_b32 v209, v186 offset:16520
	ds_write_b32 v209, v187 offset:16524
	s_waitcnt vmcnt(4)
	ds_write_b32 v209, v188 offset:24768
	ds_write_b32 v209, v189 offset:24772
	ds_write_b32 v209, v190 offset:24776
	ds_write_b32 v209, v191 offset:24780
	s_waitcnt vmcnt(3)
	ds_write_b32 v209, v192 offset:33024
	ds_write_b32 v209, v193 offset:33028
	ds_write_b32 v209, v194 offset:33032
	ds_write_b32 v209, v195 offset:33036
	s_waitcnt vmcnt(2)
	ds_write_b32 v209, v196 offset:41280
	ds_write_b32 v209, v197 offset:41284
	ds_write_b32 v209, v198 offset:41288
	ds_write_b32 v209, v199 offset:41292
	s_waitcnt vmcnt(1)
	ds_write_b32 v209, v200 offset:49536
	ds_write_b32 v209, v201 offset:49540
	ds_write_b32 v209, v202 offset:49544
	ds_write_b32 v209, v203 offset:49548
	s_waitcnt vmcnt(0)
	ds_write_b32 v209, v204 offset:57792
	ds_write_b32 v209, v205 offset:57796
	ds_write_b32 v209, v206 offset:57800
	ds_write_b32 v209, v207 offset:57804
	s_waitcnt lgkmcnt(0)
	s_barrier
; #define LAS __attribute__((address_space(3)))
; __device__ __forceinline__ void lds_barrier() { asm volatile("s_waitcnt lgkmcnt(0)" ::: "memory"); __builtin_amdgcn_s_barrier(); asm volatile("" ::: "memory"); }
; __device__ __forceinline__ void phase_prologue(const Args& a, LAS unsigned char* lds) {
;     ...
;         lds_barrier();
; #pragma unroll
;         for (int i = 0; i < 4; ++i) { const int piece = tid + 512 * i, nl = piece >> 4, kg = piece & 15; const LAS float* s = tile + (kg * 8) * 129 + nl;
;             u32x4 o; o.x = pk2(s[0], s[129]); o.y = pk2(s[258], s[387]); o.z = pk2(s[516], s[645]); o.w = pk2(s[774], s[903]);
;             *(u32x4*)(dst + (size_t)(drow0 + nl) * 2048 + k0 + kg * 8) = o; }
	ds_read_b32 v160, v114
	ds_read_b32 v161, v114 offset:516
	ds_read_b32 v162, v114 offset:1032
	ds_read_b32 v163, v114 offset:1548
	ds_read_b32 v164, v114 offset:2064
	ds_read_b32 v165, v114 offset:2580
	ds_read_b32 v166, v114 offset:3096
	ds_read_b32 v167, v114 offset:3612
	s_waitcnt lgkmcnt(0)
	v_cvt_pk_bf16_f32 v168, v160, v161
	v_cvt_pk_bf16_f32 v169, v162, v163
	v_cvt_pk_bf16_f32 v170, v164, v165
	v_cvt_pk_bf16_f32 v171, v166, v167
	global_store_dwordx4 v115, v[168:171], s[28:29]
	ds_read_b32 v160, v114 offset:128
	ds_read_b32 v161, v114 offset:644
	ds_read_b32 v162, v114 offset:1160
	ds_read_b32 v163, v114 offset:1676
	ds_read_b32 v164, v114 offset:2192
	ds_read_b32 v165, v114 offset:2708
	ds_read_b32 v166, v114 offset:3224
	ds_read_b32 v167, v114 offset:3740
	s_waitcnt lgkmcnt(0)
	v_cvt_pk_bf16_f32 v172, v160, v161
	v_cvt_pk_bf16_f32 v173, v162, v163
	v_cvt_pk_bf16_f32 v174, v164, v165
	v_cvt_pk_bf16_f32 v175, v166, v167
	global_store_dwordx4 v116, v[172:175], s[28:29]
	ds_read_b32 v160, v114 offset:256
	ds_read_b32 v161, v114 offset:772
	ds_read_b32 v162, v114 offset:1288
	ds_read_b32 v163, v114 offset:1804
	ds_read_b32 v164, v114 offset:2320
	ds_read_b32 v165, v114 offset:2836
	ds_read_b32 v166, v114 offset:3352
	ds_read_b32 v167, v114 offset:3868
	s_waitcnt lgkmcnt(0)
	v_cvt_pk_bf16_f32 v168, v160, v161
	v_cvt_pk_bf16_f32 v169, v162, v163
	v_cvt_pk_bf16_f32 v170, v164, v165
	v_cvt_pk_bf16_f32 v171, v166, v167
	global_store_dwordx4 v117, v[168:171], s[28:29]
	ds_read_b32 v160, v114 offset:384
	ds_read_b32 v161, v114 offset:900
	ds_read_b32 v162, v114 offset:1416
	ds_read_b32 v163, v114 offset:1932
	ds_read_b32 v164, v114 offset:2448
	ds_read_b32 v165, v114 offset:2964
	ds_read_b32 v166, v114 offset:3480
	ds_read_b32 v167, v114 offset:3996
	s_waitcnt lgkmcnt(0)
	v_cvt_pk_bf16_f32 v172, v160, v161
	v_cvt_pk_bf16_f32 v173, v162, v163
	v_cvt_pk_bf16_f32 v174, v164, v165
	v_cvt_pk_bf16_f32 v175, v166, v167
	global_store_dwordx4 v118, v[172:175], s[28:29]
	ds_read_b32 v160, v210
	ds_read_b32 v161, v210 offset:516
	ds_read_b32 v162, v210 offset:1032
	ds_read_b32 v163, v210 offset:1548
	ds_read_b32 v164, v210 offset:2064
	ds_read_b32 v165, v210 offset:2580
	ds_read_b32 v166, v210 offset:3096
	ds_read_b32 v167, v210 offset:3612
	s_waitcnt lgkmcnt(0)
	v_cvt_pk_bf16_f32 v168, v160, v161
	v_cvt_pk_bf16_f32 v169, v162, v163
	v_cvt_pk_bf16_f32 v170, v164, v165
	v_cvt_pk_bf16_f32 v171, v166, v167
	global_store_dwordx4 v115, v[168:171], s[44:45]
	ds_read_b32 v160, v210 offset:128
	ds_read_b32 v161, v210 offset:644
	ds_read_b32 v162, v210 offset:1160
	ds_read_b32 v163, v210 offset:1676
	ds_read_b32 v164, v210 offset:2192
	ds_read_b32 v165, v210 offset:2708
	ds_read_b32 v166, v210 offset:3224
	ds_read_b32 v167, v210 offset:3740
	s_waitcnt lgkmcnt(0)
	v_cvt_pk_bf16_f32 v172, v160, v161
	v_cvt_pk_bf16_f32 v173, v162, v163
	v_cvt_pk_bf16_f32 v174, v164, v165
	v_cvt_pk_bf16_f32 v175, v166, v167
	global_store_dwordx4 v116, v[172:175], s[44:45]
	ds_read_b32 v160, v210 offset:256
	ds_read_b32 v161, v210 offset:772
	ds_read_b32 v162, v210 offset:1288
	ds_read_b32 v163, v210 offset:1804
	ds_read_b32 v164, v210 offset:2320
	ds_read_b32 v165, v210 offset:2836
	ds_read_b32 v166, v210 offset:3352
	ds_read_b32 v167, v210 offset:3868
	s_waitcnt lgkmcnt(0)
	v_cvt_pk_bf16_f32 v168, v160, v161
	v_cvt_pk_bf16_f32 v169, v162, v163
	v_cvt_pk_bf16_f32 v170, v164, v165
	v_cvt_pk_bf16_f32 v171, v166, v167
	global_store_dwordx4 v117, v[168:171], s[44:45]
	ds_read_b32 v160, v210 offset:384
	ds_read_b32 v161, v210 offset:900
	ds_read_b32 v162, v210 offset:1416
	ds_read_b32 v163, v210 offset:1932
	ds_read_b32 v164, v210 offset:2448
	ds_read_b32 v165, v210 offset:2964
	ds_read_b32 v166, v210 offset:3480
	ds_read_b32 v167, v210 offset:3996
	s_waitcnt lgkmcnt(0)
	v_cvt_pk_bf16_f32 v172, v160, v161
	v_cvt_pk_bf16_f32 v173, v162, v163
	v_cvt_pk_bf16_f32 v174, v164, v165
	v_cvt_pk_bf16_f32 v175, v166, v167
	global_store_dwordx4 v118, v[172:175], s[44:45]
	s_cmpk_ge_u32 s25, 0x100
	s_cbranch_scc1 .Lcvb_done
	v_cmp_eq_u32_e32 vcc, 0, v0
	s_and_saveexec_b64 s[34:35], vcc
	s_cbranch_execz .Lcvb_t0c
	s_waitcnt vmcnt(0)
	ds_write_b32 v125, v123
	ds_write_b32 v125, v124 offset:4

; #define LAS __attribute__((address_space(3)))
; __device__ __forceinline__ void phase_prologue(const Args& a, LAS unsigned char* lds) {
;     ...
;     unsigned* cq_head = (unsigned*)(a.ws + WS_CTL) + 8192 + 768;
;     volatile LAS int* qs = (volatile LAS int*)(lds + 128 * 129 * 4);
;     int pend = 0, it = 0;
;     if (tid == 0) { qs[0] = (int)xb_add(cq_head, 1u); pend = (int)xb_add(cq_head, 1u); }
;     __syncthreads();
;     for (int u = qs[0]; u < CTOT; u = qs[it & 1]) {
;         int r = u; const float* src; int ldn, nvalid, NT, mode = 0; bf16_t* dst;
;         if (r < CJ0) { src = a.in[I_EVIN]; ldn = 6144; nvalid = 6144; NT = 48; dst = (bf16_t*)(a.ws + WS_WIN0); }
;         else if ((r -= CJ0) < CJ1) { src = a.in[I_EVOUT]; ldn = 2048; nvalid = 2048; NT = 16; dst = (bf16_t*)(a.ws + WS_WOUT0); }
;         else if ((r -= CJ1) < CJ2) { src = a.in[I_ODIN]; ldn = 6176; nvalid = 6176; NT = 50; dst = (bf16_t*)(a.ws + WS_WIN1); }
;         else if ((r -= CJ2) < CJ3) { src = a.in[I_ODOUT]; ldn = 2048; nvalid = 2048; NT = 16; dst = (bf16_t*)(a.ws + WS_WOUT1); }
;         else { r -= CJ3; const int which = r / CJM; r -= which * CJM; const int mtx = r >> 8; r &= 255; ldn = 2048; nvalid = 2048; NT = 16;
;             if (which == 0) { src = a.in[I_WGATE] + (size_t)mtx * 2048 * 2048; dst = (bf16_t*)(a.ws + WS_WGU) + (size_t)mtx * 4096 * 2048; mode = 1; }
;             else if (which == 1) { src = a.in[I_WUP] + (size_t)mtx * 2048 * 2048; dst = (bf16_t*)(a.ws + WS_WGU) + (size_t)mtx * 4096 * 2048; mode = 2; }
;             else { src = a.in[I_WDOWN] + (size_t)mtx * 2048 * 2048; dst = (bf16_t*)(a.ws + WS_WDN) + (size_t)mtx * 2048 * 2048; } }
;         const int kt = r / NT, ntl = r % NT, k0 = kt * 128, n0 = ntl * 128;
;         const int drow0 = mode == 0 ? n0 : (ntl * 256 + (mode == 2 ? 128 : 0));
;         f32x4 v[8];
; #pragma unroll
;         for (int i = 0; i < 8; ++i) { const int id = tid + 512 * i, row = id >> 5, c4 = id & 31, n = n0 + c4 * 4;
;             v[i] = (f32x4){0.f, 0.f, 0.f, 0.f};
;             if (n < nvalid) v[i] = *(const f32x4*)(src + (size_t)(k0 + row) * ldn + n); }
; #pragma unroll
;         for (int i = 0; i < 8; ++i) { const int id = tid + 512 * i, row = id >> 5, c4 = id & 31;
;             LAS float* tp = tile + row * 129 + c4 * 4; tp[0] = v[i][0]; tp[1] = v[i][1]; tp[2] = v[i][2]; tp[3] = v[i][3]; }
;         lds_barrier();
; #pragma unroll
.LBB0_1648:
.Lcvz_entry:
	s_waitcnt vmcnt(0) lgkmcnt(0)
	s_barrier
	v_mov_b32_e32 v119, 1
	v_mov_b32_e32 v208, 2
	v_mov_b32_e32 v120, 0x9000
	v_mov_b32_e32 v122, 0
	v_mov_b32_e32 v125, 0x10200
	s_mov_b32 s25, 0
	v_lshrrev_b32_e32 v104, 5, v0
	v_and_b32_e32 v126, 31, v0
	v_lshlrev_b32_e32 v105, 13, v104
	v_lshl_add_u32 v105, v126, 4, v105
	v_add_u32_e32 v106, 0x20000, v105
	v_add_u32_e32 v107, 0x40000, v105
	v_add_u32_e32 v108, 0x60000, v105
	v_add_u32_e32 v109, 0x80000, v105
	v_add_u32_e32 v110, 0xa0000, v105
	v_add_u32_e32 v111, 0xc0000, v105
	v_add_u32_e32 v112, 0xe0000, v105
	v_mul_u32_u24_e32 v113, 0x204, v104
	v_lshl_add_u32 v113, v126, 4, v113
	v_lshrrev_b32_e32 v127, 4, v0
	v_and_b32_e32 v126, 15, v0
	v_mul_u32_u24_e32 v114, 0x1020, v126
	v_lshl_add_u32 v114, v127, 2, v114
	v_lshlrev_b32_e32 v115, 12, v127
	v_lshl_add_u32 v115, v126, 4, v115
	v_add_u32_e32 v116, 0x20000, v115
	v_add_u32_e32 v117, 0x40000, v115
	v_add_u32_e32 v118, 0x60000, v115
	v_add_u32_e32 v209, 0x10240, v113
	v_add_u32_e32 v210, 0x10240, v114
	v_readlane_b32 s42, v254, 27
	v_readlane_b32 s43, v254, 28
	s_sub_u32 s42, s42, 0x28
	s_subb_u32 s43, s43, 0
	s_load_dwordx2 s[40:41], s[42:43], 0x0
	s_waitcnt lgkmcnt(0)
	v_cmp_eq_u32_e32 vcc, 0, v0
	s_and_saveexec_b64 s[34:35], vcc
	s_cbranch_execz .Lcvz_t0a
	global_atomic_add v123, v120, v208, s[94:95] sc0
	s_waitcnt vmcnt(0)
	ds_write_b32 v125, v123

; #define LAS __attribute__((address_space(3)))
; __device__ __forceinline__ void lds_barrier() { asm volatile("s_waitcnt lgkmcnt(0)" ::: "memory"); __builtin_amdgcn_s_barrier(); asm volatile("" ::: "memory"); }
; __device__ __forceinline__ void phase_prologue(const Args& a, LAS unsigned char* lds) {
;     ...
;         int r = u; const float* src; int ldn, nvalid, NT, mode = 0; bf16_t* dst;
;         if (r < CJ0) { src = a.in[I_EVIN]; ldn = 6144; nvalid = 6144; NT = 48; dst = (bf16_t*)(a.ws + WS_WIN0); }
;         else if ((r -= CJ0) < CJ1) { src = a.in[I_EVOUT]; ldn = 2048; nvalid = 2048; NT = 16; dst = (bf16_t*)(a.ws + WS_WOUT0); }
;         else if ((r -= CJ1) < CJ2) { src = a.in[I_ODIN]; ldn = 6176; nvalid = 6176; NT = 50; dst = (bf16_t*)(a.ws + WS_WIN1); }
;         else if ((r -= CJ2) < CJ3) { src = a.in[I_ODOUT]; ldn = 2048; nvalid = 2048; NT = 16; dst = (bf16_t*)(a.ws + WS_WOUT1); }
;         else { r -= CJ3; const int which = r / CJM; r -= which * CJM; const int mtx = r >> 8; r &= 255; ldn = 2048; nvalid = 2048; NT = 16;
;             if (which == 0) { src = a.in[I_WGATE] + (size_t)mtx * 2048 * 2048; dst = (bf16_t*)(a.ws + WS_WGU) + (size_t)mtx * 4096 * 2048; mode = 1; }
;             else if (which == 1) { src = a.in[I_WUP] + (size_t)mtx * 2048 * 2048; dst = (bf16_t*)(a.ws + WS_WGU) + (size_t)mtx * 4096 * 2048; mode = 2; }
;             else { src = a.in[I_WDOWN] + (size_t)mtx * 2048 * 2048; dst = (bf16_t*)(a.ws + WS_WDN) + (size_t)mtx * 2048 * 2048; } }
;         const int kt = r / NT, ntl = r % NT, k0 = kt * 128, n0 = ntl * 128;
;         const int drow0 = mode == 0 ? n0 : (ntl * 256 + (mode == 2 ? 128 : 0));
;         f32x4 v[8];
; #pragma unroll
;         for (int i = 0; i < 8; ++i) { const int id = tid + 512 * i, row = id >> 5, c4 = id & 31, n = n0 + c4 * 4;
;             v[i] = (f32x4){0.f, 0.f, 0.f, 0.f};
;             if (n < nvalid) v[i] = *(const f32x4*)(src + (size_t)(k0 + row) * ldn + n); }
; #pragma unroll
;         for (int i = 0; i < 8; ++i) { const int id = tid + 512 * i, row = id >> 5, c4 = id & 31;
;             LAS float* tp = tile + row * 129 + c4 * 4; tp[0] = v[i][0]; tp[1] = v[i][1]; tp[2] = v[i][2]; tp[3] = v[i][3]; }
;         lds_barrier();
.Lcvz_loop:
	ds_read_b32 v126, v125
	s_waitcnt lgkmcnt(0)
	v_readfirstlane_b32 s24, v126
	s_cmpk_gt_u32 s24, 0x1fff
	s_cbranch_scc1 .Lcvz_done
	v_cmp_eq_u32_e32 vcc, 0, v0
	s_and_saveexec_b64 s[34:35], vcc
	s_cbranch_execz .Lcvz_t0b
	global_atomic_add v123, v120, v208, s[94:95] sc0
.Lcvz_t0b:
	s_mov_b64 exec, s[34:35]
	s_lshr_b32 s36, s24, 12
	s_bfe_u32 s30, s24, 0x40008
	s_add_i32 s30, s30, 16
	s_lshl_b32 s30, s30, 24
	s_bfe_u32 s31, s24, 0x40004
	s_and_b32 s32, s24, 15
	v_readlane_b32 s26, v254, 43
	v_readlane_b32 s27, v254, 44
	s_cmp_lg_u32 s36, 0
	s_cselect_b32 s26, s40, s26
	s_cselect_b32 s27, s41, s27
	s_lshl_b32 s33, s31, 20
	s_add_i32 s33, s33, s30
	s_lshl_b32 s37, s32, 9
	s_add_i32 s33, s33, s37
	s_add_u32 s26, s26, s33
	s_addc_u32 s27, s27, 0
	v_readlane_b32 s28, v254, 25
	v_readlane_b32 s29, v254, 26
	s_lshl_b32 s33, s32, 20
	s_add_i32 s33, s33, s30
	s_lshl_b32 s37, s36, 19
	s_add_i32 s33, s33, s37
	s_lshl_b32 s37, s31, 8
	s_add_i32 s33, s33, s37
	s_add_u32 s28, s28, s33
	s_addc_u32 s29, s29, 0
	s_add_u32 s44, s28, 0x100000
	s_addc_u32 s45, s29, 0
	global_load_dwordx4 v[128:131], v105, s[26:27]
	global_load_dwordx4 v[132:135], v106, s[26:27]
	global_load_dwordx4 v[136:139], v107, s[26:27]
	global_load_dwordx4 v[140:143], v108, s[26:27]
	global_load_dwordx4 v[144:147], v109, s[26:27]
	global_load_dwordx4 v[148:151], v110, s[26:27]
	global_load_dwordx4 v[152:155], v111, s[26:27]
	global_load_dwordx4 v[156:159], v112, s[26:27]
	global_load_dwordx4 v[176:179], v105, s[26:27] offset:512
	global_load_dwordx4 v[180:183], v106, s[26:27] offset:512
	global_load_dwordx4 v[184:187], v107, s[26:27] offset:512
	global_load_dwordx4 v[188:191], v108, s[26:27] offset:512
	global_load_dwordx4 v[192:195], v109, s[26:27] offset:512
	global_load_dwordx4 v[196:199], v110, s[26:27] offset:512
	global_load_dwordx4 v[200:203], v111, s[26:27] offset:512
	global_load_dwordx4 v[204:207], v112, s[26:27] offset:512
	s_waitcnt vmcnt(15)
	ds_write_b32 v113, v128
	ds_write_b32 v113, v129 offset:4
	ds_write_b32 v113, v130 offset:8
	ds_write_b32 v113, v131 offset:12
	s_waitcnt vmcnt(14)
	ds_write_b32 v113, v132 offset:8256
	ds_write_b32 v113, v133 offset:8260
	ds_write_b32 v113, v134 offset:8264
	ds_write_b32 v113, v135 offset:8268
	s_waitcnt vmcnt(13)
	ds_write_b32 v113, v136 offset:16512
	ds_write_b32 v113, v137 offset:16516
	ds_write_b32 v113, v138 offset:16520
	ds_write_b32 v113, v139 offset:16524
	s_waitcnt vmcnt(12)
	ds_write_b32 v113, v140 offset:24768
	ds_write_b32 v113, v141 offset:24772
	ds_write_b32 v113, v142 offset:24776
	ds_write_b32 v113, v143 offset:24780
	s_waitcnt vmcnt(11)
	ds_write_b32 v113, v144 offset:33024
	ds_write_b32 v113, v145 offset:33028
	ds_write_b32 v113, v146 offset:33032
	ds_write_b32 v113, v147 offset:33036
	s_waitcnt vmcnt(10)
	ds_write_b32 v113, v148 offset:41280
	ds_write_b32 v113, v149 offset:41284
	ds_write_b32 v113, v150 offset:41288
	ds_write_b32 v113, v151 offset:41292
	s_waitcnt vmcnt(9)
	ds_write_b32 v113, v152 offset:49536
	ds_write_b32 v113, v153 offset:49540
	ds_write_b32 v113, v154 offset:49544
	ds_write_b32 v113, v155 offset:49548
	s_waitcnt vmcnt(8)
	ds_write_b32 v113, v156 offset:57792
	ds_write_b32 v113, v157 offset:57796
	ds_write_b32 v113, v158 offset:57800
	ds_write_b32 v113, v159 offset:57804
	s_waitcnt vmcnt(7)
	ds_write_b32 v209, v176
	ds_write_b32 v209, v177 offset:4
	ds_write_b32 v209, v178 offset:8
	ds_write_b32 v209, v179 offset:12
	s_waitcnt vmcnt(6)
	ds_write_b32 v209, v180 offset:8256
	ds_write_b32 v209, v181 offset:8260
	ds_write_b32 v209, v182 offset:8264
	ds_write_b32 v209, v183 offset:8268
	s_waitcnt vmcnt(5)
	ds_write_b32 v209, v184 offset:16512
	ds_write_b32 v209, v185 offset:16516
	ds_write_b32 v209, v186 offset:16520
	ds_write_b32 v209, v187 offset:16524
	s_waitcnt vmcnt(4)
	ds_write_b32 v209, v188 offset:24768
	ds_write_b32 v209, v189 offset:24772
	ds_write_b32 v209, v190 offset:24776
	ds_write_b32 v209, v191 offset:24780
	s_waitcnt vmcnt(3)
	ds_write_b32 v209, v192 offset:33024
	ds_write_b32 v209, v193 offset:33028
	ds_write_b32 v209, v194 offset:33032
	ds_write_b32 v209, v195 offset:33036
	s_waitcnt vmcnt(2)
	ds_write_b32 v209, v196 offset:41280
	ds_write_b32 v209, v197 offset:41284
	ds_write_b32 v209, v198 offset:41288
	ds_write_b32 v209, v199 offset:41292
	s_waitcnt vmcnt(1)
	ds_write_b32 v209, v200 offset:49536
	ds_write_b32 v209, v201 offset:49540
	ds_write_b32 v209, v202 offset:49544
	ds_write_b32 v209, v203 offset:49548
	s_waitcnt vmcnt(0)
	ds_write_b32 v209, v204 offset:57792
	ds_write_b32 v209, v205 offset:57796
	ds_write_b32 v209, v206 offset:57800
	ds_write_b32 v209, v207 offset:57804
	s_waitcnt lgkmcnt(0)
	s_barrier
; #define LAS __attribute__((address_space(3)))
; __device__ __forceinline__ void lds_barrier() { asm volatile("s_waitcnt lgkmcnt(0)" ::: "memory"); __builtin_amdgcn_s_barrier(); asm volatile("" ::: "memory"); }
; __device__ __forceinline__ unsigned xb_add(unsigned* p, unsigned v) { return __hip_atomic_fetch_add(p, v, __ATOMIC_RELAXED, __HIP_MEMORY_SCOPE_AGENT); }
; __device__ __forceinline__ void phase_prologue(const Args& a, LAS unsigned char* lds) {
;     ...
;         lds_barrier();
; #pragma unroll
;         for (int i = 0; i < 4; ++i) { const int piece = tid + 512 * i, nl = piece >> 4, kg = piece & 15; const LAS float* s = tile + (kg * 8) * 129 + nl;
;             u32x4 o; o.x = pk2(s[0], s[129]); o.y = pk2(s[258], s[387]); o.z = pk2(s[516], s[645]); o.w = pk2(s[774], s[903]);
;             *(u32x4*)(dst + (size_t)(drow0 + nl) * 2048 + k0 + kg * 8) = o; }
;         ++it;
;         if (tid == 0) { qs[it & 1] = pend; pend = (int)xb_add(cq_head, 1u); }
;         lds_barrier();
	ds_read_b32 v160, v114
	ds_read_b32 v161, v114 offset:516
	ds_read_b32 v162, v114 offset:1032
	ds_read_b32 v163, v114 offset:1548
	ds_read_b32 v164, v114 offset:2064
	ds_read_b32 v165, v114 offset:2580
	ds_read_b32 v166, v114 offset:3096
	ds_read_b32 v167, v114 offset:3612
	s_waitcnt lgkmcnt(0)
	v_cvt_pk_bf16_f32 v168, v160, v161
	v_cvt_pk_bf16_f32 v169, v162, v163
	v_cvt_pk_bf16_f32 v170, v164, v165
	v_cvt_pk_bf16_f32 v171, v166, v167
	global_store_dwordx4 v115, v[168:171], s[28:29]
	ds_read_b32 v160, v114 offset:128
	ds_read_b32 v161, v114 offset:644
	ds_read_b32 v162, v114 offset:1160
	ds_read_b32 v163, v114 offset:1676
	ds_read_b32 v164, v114 offset:2192
	ds_read_b32 v165, v114 offset:2708
	ds_read_b32 v166, v114 offset:3224
	ds_read_b32 v167, v114 offset:3740
	s_waitcnt lgkmcnt(0)
	v_cvt_pk_bf16_f32 v172, v160, v161
	v_cvt_pk_bf16_f32 v173, v162, v163
	v_cvt_pk_bf16_f32 v174, v164, v165
	v_cvt_pk_bf16_f32 v175, v166, v167
	global_store_dwordx4 v116, v[172:175], s[28:29]
	ds_read_b32 v160, v114 offset:256
	ds_read_b32 v161, v114 offset:772
	ds_read_b32 v162, v114 offset:1288
	ds_read_b32 v163, v114 offset:1804
	ds_read_b32 v164, v114 offset:2320
	ds_read_b32 v165, v114 offset:2836
	ds_read_b32 v166, v114 offset:3352
	ds_read_b32 v167, v114 offset:3868
	s_waitcnt lgkmcnt(0)
	v_cvt_pk_bf16_f32 v168, v160, v161
	v_cvt_pk_bf16_f32 v169, v162, v163
	v_cvt_pk_bf16_f32 v170, v164, v165
	v_cvt_pk_bf16_f32 v171, v166, v167
	global_store_dwordx4 v117, v[168:171], s[28:29]
	ds_read_b32 v160, v114 offset:384
	ds_read_b32 v161, v114 offset:900
	ds_read_b32 v162, v114 offset:1416
	ds_read_b32 v163, v114 offset:1932
	ds_read_b32 v164, v114 offset:2448
	ds_read_b32 v165, v114 offset:2964
	ds_read_b32 v166, v114 offset:3480
	ds_read_b32 v167, v114 offset:3996
	s_waitcnt lgkmcnt(0)
	v_cvt_pk_bf16_f32 v172, v160, v161
	v_cvt_pk_bf16_f32 v173, v162, v163
	v_cvt_pk_bf16_f32 v174, v164, v165
	v_cvt_pk_bf16_f32 v175, v166, v167
	global_store_dwordx4 v118, v[172:175], s[28:29]
	ds_read_b32 v160, v210
	ds_read_b32 v161, v210 offset:516
	ds_read_b32 v162, v210 offset:1032
	ds_read_b32 v163, v210 offset:1548
	ds_read_b32 v164, v210 offset:2064
	ds_read_b32 v165, v210 offset:2580
	ds_read_b32 v166, v210 offset:3096
	ds_read_b32 v167, v210 offset:3612
	s_waitcnt lgkmcnt(0)
	v_cvt_pk_bf16_f32 v168, v160, v161
	v_cvt_pk_bf16_f32 v169, v162, v163
	v_cvt_pk_bf16_f32 v170, v164, v165
	v_cvt_pk_bf16_f32 v171, v166, v167
	global_store_dwordx4 v115, v[168:171], s[44:45]
	ds_read_b32 v160, v210 offset:128
	ds_read_b32 v161, v210 offset:644
	ds_read_b32 v162, v210 offset:1160
	ds_read_b32 v163, v210 offset:1676
	ds_read_b32 v164, v210 offset:2192
	ds_read_b32 v165, v210 offset:2708
	ds_read_b32 v166, v210 offset:3224
	ds_read_b32 v167, v210 offset:3740
	s_waitcnt lgkmcnt(0)
	v_cvt_pk_bf16_f32 v172, v160, v161
	v_cvt_pk_bf16_f32 v173, v162, v163
	v_cvt_pk_bf16_f32 v174, v164, v165
	v_cvt_pk_bf16_f32 v175, v166, v167
	global_store_dwordx4 v116, v[172:175], s[44:45]
	ds_read_b32 v160, v210 offset:256
	ds_read_b32 v161, v210 offset:772
	ds_read_b32 v162, v210 offset:1288
	ds_read_b32 v163, v210 offset:1804
	ds_read_b32 v164, v210 offset:2320
	ds_read_b32 v165, v210 offset:2836
	ds_read_b32 v166, v210 offset:3352
	ds_read_b32 v167, v210 offset:3868
	s_waitcnt lgkmcnt(0)
	v_cvt_pk_bf16_f32 v168, v160, v161
	v_cvt_pk_bf16_f32 v169, v162, v163
	v_cvt_pk_bf16_f32 v170, v164, v165
	v_cvt_pk_bf16_f32 v171, v166, v167
	global_store_dwordx4 v117, v[168:171], s[44:45]
	ds_read_b32 v160, v210 offset:384
	ds_read_b32 v161, v210 offset:900
	ds_read_b32 v162, v210 offset:1416
	ds_read_b32 v163, v210 offset:1932
	ds_read_b32 v164, v210 offset:2448
	ds_read_b32 v165, v210 offset:2964
	ds_read_b32 v166, v210 offset:3480
	ds_read_b32 v167, v210 offset:3996
	s_waitcnt lgkmcnt(0)
	v_cvt_pk_bf16_f32 v172, v160, v161
	v_cvt_pk_bf16_f32 v173, v162, v163
	v_cvt_pk_bf16_f32 v174, v164, v165
	v_cvt_pk_bf16_f32 v175, v166, v167
	global_store_dwordx4 v118, v[172:175], s[44:45]
	v_cmp_eq_u32_e32 vcc, 0, v0
	s_and_saveexec_b64 s[34:35], vcc
	s_cbranch_execz .Lcvz_t0c
	s_waitcnt vmcnt(0)
	ds_write_b32 v125, v123
